# one-atomic quota reservation with all layer-1 tiles deferred, idle-slot quotas 7/11/10/12
# baseline (speedup 1.0000x reference)
; #define SEAM(k) do { if (IN(k) && IN((k) + 1)) xcd_barrier(bar); \
;         if (PROBE_MASK) { const unsigned long long t_ = __builtin_amdgcn_s_memrealtime(); if ((PROBE_MASK >> (k)) & 1u) pr_acc += t_ - pr_t0; pr_t0 = t_; } } while (0)
; __device__ __forceinline__ void convert_deferred(const Ptrs& P, unsigned char* lds, int quota) {
;     const int tid = threadIdx.x, wid = tid >> 6, lane = tid & 63;
;     float* tile = (float*)lds;
;     volatile __attribute__((address_space(3))) int* slot = (volatile __attribute__((address_space(3))) int*)((__attribute__((address_space(3))) unsigned char*)lds + 131072 + 320 + 11000);
;     unsigned* q = (unsigned*)(P.ws + WS_CTL) + CW_DEFQ;
;     for (int n = 0; n < quota; ++n) {
;         __syncthreads();
;         if (tid == 0) *slot = (int)atomicAdd(q, 1u);
;         __syncthreads();
;         const int t = *slot;
;         if (t >= DEF_GU + DEF_DN) break;
;         const bool gu = t < DEF_GU;
;         const float* src = gu ? P.in[34] : P.in[36]; bf16* dst = (bf16*)(P.ws + (gu ? WS_WGU : WS_WDN));
;         const int N = gu ? 2048 : 1024, ntn = N / 256, it = gu ? 2 * NE * 16 * 8 - DEF_GU + t : 2 * NE * 16 * 4 - DEF_DN + (t - DEF_GU);
; __global__ void __launch_bounds__(NT, 2) mega(Args args) {
;     ...
;         if (IDLE_LAST(68 * 7)) convert_deferred(P, lds, 4); } SEAM(2);
.LBB0_779:
	s_abs_i32 s3, s62
	v_cvt_f32_u32_e32 v2, s3
	s_sub_i32 s4, 0, s3
	s_mov_b32 s5, 0
	v_rcp_iflag_f32_e32 v2, v2
	s_nop 0
	v_mul_f32_e32 v2, 0x4f7ffffe, v2
	v_cvt_u32_f32_e32 v2, v2
	s_nop 0
	v_readfirstlane_b32 s6, v2
	s_mul_i32 s4, s4, s6
	s_mul_hi_u32 s4, s6, s4
	s_add_i32 s6, s6, s4
	s_mul_hi_u32 s4, s6, 0x1dc
	s_mul_i32 s4, s4, s3
	s_sub_i32 s4, 0x1dc, s4
	s_sub_i32 s6, s4, s3
	s_cmp_ge_u32 s4, s3
	s_cselect_b32 s4, s6, s4
	s_sub_i32 s6, s4, s3
	s_cmp_ge_u32 s4, s3
	s_cselect_b32 s3, s6, s4
	s_cmp_eq_u32 s3, 0
	s_cselect_b64 s[6:7], -1, 0
	s_cmp_lt_i32 s2, s3
	s_cselect_b64 s[8:9], -1, 0
	s_or_b64 s[6:7], s[6:7], s[8:9]
	s_and_b64 vcc, exec, s[6:7]
	s_cbranch_vccnz .LBB0_789
	v_and_b32_e32 v2, 0x7c, v155
	v_lshlrev_b32_e32 v3, 5, v0
	s_movk_i32 s3, 0x400
	v_lshrrev_b32_e32 v4, 6, v0
	v_and_or_b32 v12, v3, s3, v2
	v_bfe_u32 v2, v0, 3, 3
	v_lshl_or_b32 v5, v4, 5, v2
	v_lshlrev_b32_e32 v2, 3, v0
	v_lshl_add_u32 v11, v182, 4, 0
	v_and_b32_e32 v2, 56, v2
	v_mul_u32_u24_e32 v16, 0x2020, v4
	v_mov_b32_e32 v3, 0
	v_lshl_add_u32 v27, v5, 2, 0
	v_mul_u32_u24_e32 v28, 0x404, v2
	v_lshlrev_b32_e32 v10, 6, v5
	s_add_i32 s12, 0, 0x22c38
	v_add_u32_e32 v16, v11, v16
	v_and_b32_e32 v13, 0xfc, v155
	v_and_b32_e32 v14, 56, v154
	s_mov_b32 s3, 7
	s_mov_b32 s91, 0
	v_or_b32_e32 v4, 0x200, v10
	v_mov_b32_e32 v5, v3
	v_or_b32_e32 v6, 0x400, v10
	v_mov_b32_e32 v7, v3
	v_or_b32_e32 v8, 0x600, v10
	v_mov_b32_e32 v9, v3
	v_mov_b32_e32 v15, s12
	s_movk_i32 s13, 0x17ff
	s_movk_i32 s14, 0x800
	s_mov_b32 s15, 0x1104e000
	s_movk_i32 s16, -2048
	v_add_u32_e32 v17, 0x404, v16
	v_add_u32_e32 v18, 0x40c, v16
	v_add_u32_e32 v19, 0x808, v16
	v_add_u32_e32 v20, 0xc0c, v16
	v_add_u32_e32 v21, 0xc14, v16
	v_add_u32_e32 v22, 0x1414, v16
	v_add_u32_e32 v23, 0x141c, v16
	v_add_u32_e32 v24, 0x1818, v16
	v_add_u32_e32 v25, 0x1c1c, v16
	v_add_u32_e32 v26, 0x1c24, v16
	v_lshlrev_b32_e32 v2, 1, v2
	v_add_u32_e32 v27, v27, v28
	v_lshlrev_b32_e32 v10, 1, v10
	s_branch .LBB0_782

; #define SEAM(k) do { if (IN(k) && IN((k) + 1)) xcd_barrier(bar); \
;         if (PROBE_MASK) { const unsigned long long t_ = __builtin_amdgcn_s_memrealtime(); if ((PROBE_MASK >> (k)) & 1u) pr_acc += t_ - pr_t0; pr_t0 = t_; } } while (0)
; __device__ __forceinline__ void convert_deferred(const Ptrs& P, unsigned char* lds, int quota) {
;     const int tid = threadIdx.x, wid = tid >> 6, lane = tid & 63;
;     float* tile = (float*)lds;
;     volatile __attribute__((address_space(3))) int* slot = (volatile __attribute__((address_space(3))) int*)((__attribute__((address_space(3))) unsigned char*)lds + 131072 + 320 + 11000);
;     unsigned* q = (unsigned*)(P.ws + WS_CTL) + CW_DEFQ;
;     for (int n = 0; n < quota; ++n) {
;         __syncthreads();
;         if (tid == 0) *slot = (int)atomicAdd(q, 1u);
;         __syncthreads();
;         const int t = *slot;
;         if (t >= DEF_GU + DEF_DN) break;
;         const bool gu = t < DEF_GU;
;         const float* src = gu ? P.in[34] : P.in[36]; bf16* dst = (bf16*)(P.ws + (gu ? WS_WGU : WS_WDN));
;         const int N = gu ? 2048 : 1024, ntn = N / 256, it = gu ? 2 * NE * 16 * 8 - DEF_GU + t : 2 * NE * 16 * 4 - DEF_DN + (t - DEF_GU);
; __global__ void __launch_bounds__(NT, 2) mega(Args args) {
;     ...
;         if (IDLE_LAST(68 * 4)) convert_deferred(P, lds, 4); } SEAM(6);
.LBB0_1286:
	s_abs_i32 s3, s62
	v_cvt_f32_u32_e32 v2, s3
	s_sub_i32 s4, 0, s3
	s_mov_b32 s5, 0
	v_rcp_iflag_f32_e32 v2, v2
	s_nop 0
	v_mul_f32_e32 v2, 0x4f7ffffe, v2
	v_cvt_u32_f32_e32 v2, v2
	s_nop 0
	v_readfirstlane_b32 s6, v2
	s_mul_i32 s4, s4, s6
	s_mul_hi_u32 s4, s6, s4
	s_add_i32 s6, s6, s4
	s_mul_hi_u32 s4, s6, 0x110
	s_mul_i32 s4, s4, s3
	s_sub_i32 s4, 0x110, s4
	s_sub_i32 s6, s4, s3
	s_cmp_ge_u32 s4, s3
	s_cselect_b32 s4, s6, s4
	s_sub_i32 s6, s4, s3
	s_cmp_ge_u32 s4, s3
	s_cselect_b32 s3, s6, s4
	s_cmp_eq_u32 s3, 0
	s_cselect_b64 s[6:7], -1, 0
	s_cmp_lt_i32 s2, s3
	s_cselect_b64 s[8:9], -1, 0
	s_or_b64 s[6:7], s[6:7], s[8:9]
	s_and_b64 vcc, exec, s[6:7]
	s_cbranch_vccnz .LBB0_1296
	v_and_b32_e32 v2, 0x7c, v188
	v_lshlrev_b32_e32 v3, 5, v0
	s_movk_i32 s3, 0x400
	v_and_or_b32 v12, v3, s3, v2
	v_bfe_u32 v2, v0, 3, 3
	v_lshl_or_b32 v4, v1, 5, v2
	v_lshlrev_b32_e32 v2, 3, v0
	v_lshl_add_u32 v11, v182, 4, 0
	v_and_b32_e32 v2, 56, v2
	v_mul_u32_u24_e32 v16, 0x2020, v1
	v_mov_b32_e32 v3, 0
	v_lshl_add_u32 v27, v4, 2, 0
	v_mul_u32_u24_e32 v28, 0x404, v2
	v_lshlrev_b32_e32 v10, 6, v4
	s_add_i32 s12, 0, 0x22c38
	v_add_u32_e32 v16, v11, v16
	v_and_b32_e32 v13, 0xfc, v188
	v_and_b32_e32 v14, 56, v185
	s_mov_b32 s3, 11
	s_mov_b32 s91, 0
	v_or_b32_e32 v4, 0x200, v10
	v_mov_b32_e32 v5, v3
	v_or_b32_e32 v6, 0x400, v10
	v_mov_b32_e32 v7, v3
	v_or_b32_e32 v8, 0x600, v10
	v_mov_b32_e32 v9, v3
	v_mov_b32_e32 v15, s12
	s_movk_i32 s13, 0x17ff
	s_movk_i32 s14, 0x800
	s_mov_b32 s15, 0x1104e000
	s_movk_i32 s16, -2048
	v_add_u32_e32 v17, 0x404, v16
	v_add_u32_e32 v18, 0x40c, v16
	v_add_u32_e32 v19, 0x808, v16
	v_add_u32_e32 v20, 0xc0c, v16
	v_add_u32_e32 v21, 0xc14, v16
	v_add_u32_e32 v22, 0x1414, v16
	v_add_u32_e32 v23, 0x141c, v16
	v_add_u32_e32 v24, 0x1818, v16
	v_add_u32_e32 v25, 0x1c1c, v16
	v_add_u32_e32 v26, 0x1c24, v16
	v_lshlrev_b32_e32 v2, 1, v2
	v_add_u32_e32 v27, v27, v28
	v_lshlrev_b32_e32 v10, 1, v10
	s_branch .LBB0_1289

; #define LAS __attribute__((address_space(3)))
; #define SEAM(k) do { if (IN(k) && IN((k) + 1)) xcd_barrier(bar); \
;         if (PROBE_MASK) { const unsigned long long t_ = __builtin_amdgcn_s_memrealtime(); if ((PROBE_MASK >> (k)) & 1u) pr_acc += t_ - pr_t0; pr_t0 = t_; } } while (0)
; __device__ __forceinline__ void convert_deferred(const Ptrs& P, unsigned char* lds, int quota) {
;     const int tid = threadIdx.x, wid = tid >> 6, lane = tid & 63;
;     float* tile = (float*)lds;
;     volatile __attribute__((address_space(3))) int* slot = (volatile __attribute__((address_space(3))) int*)((__attribute__((address_space(3))) unsigned char*)lds + 131072 + 320 + 11000);
;     unsigned* q = (unsigned*)(P.ws + WS_CTL) + CW_DEFQ;
;     for (int n = 0; n < quota; ++n) {
;         __syncthreads();
;         if (tid == 0) *slot = (int)atomicAdd(q, 1u);
;         __syncthreads();
;         const int t = *slot;
;         if (t >= DEF_GU + DEF_DN) break;
;         const bool gu = t < DEF_GU;
;         const float* src = gu ? P.in[34] : P.in[36]; bf16* dst = (bf16*)(P.ws + (gu ? WS_WGU : WS_WDN));
;         const int N = gu ? 2048 : 1024, ntn = N / 256, it = gu ? 2 * NE * 16 * 8 - DEF_GU + t : 2 * NE * 16 * 4 - DEF_DN + (t - DEF_GU);
; __global__ void __launch_bounds__(NT, 2) mega(Args args) {
;     ...
;         { const int rem_ = ((LAS int*)(LDSP + MISC_OFF + 256))[96] % G; if (rem_ != 0 && vcu >= rem_) convert_deferred(P, lds, 5); } } SEAM(9);
.LBB0_1609:
	s_abs_i32 s0, s62
	v_cvt_f32_u32_e32 v2, s0
	s_sub_i32 s5, 0, s0
	s_abs_i32 s4, s9
	s_ashr_i32 s3, s9, 31
	v_rcp_iflag_f32_e32 v2, v2
	s_mov_b32 s1, 0
	v_mul_f32_e32 v2, 0x4f7ffffe, v2
	v_cvt_u32_f32_e32 v2, v2
	s_nop 0
	v_readfirstlane_b32 s6, v2
	s_mul_i32 s5, s5, s6
	s_mul_hi_u32 s5, s6, s5
	s_add_i32 s6, s6, s5
	s_mul_hi_u32 s5, s4, s6
	s_mul_i32 s5, s5, s0
	s_sub_i32 s4, s4, s5
	s_sub_i32 s5, s4, s0
	s_cmp_ge_u32 s4, s0
	s_cselect_b32 s4, s5, s4
	s_sub_i32 s5, s4, s0
	s_cmp_ge_u32 s4, s0
	s_cselect_b32 s0, s5, s4
	s_xor_b32 s0, s0, s3
	s_sub_i32 s0, s0, s3
	s_cmp_eq_u32 s0, 0
	v_readlane_b32 s3, v254, 2
	s_cselect_b64 s[4:5], -1, 0
	s_cmp_lt_i32 s3, s0
	s_cselect_b64 s[6:7], -1, 0
	s_or_b64 s[4:5], s[4:5], s[6:7]
	s_and_b64 vcc, exec, s[4:5]
	s_cbranch_vccnz .LBB0_1619
	v_and_b32_e32 v2, 0x7c, v175
	v_lshlrev_b32_e32 v3, 5, v0
	s_movk_i32 s0, 0x400
	v_and_or_b32 v12, v3, s0, v2
	v_bfe_u32 v2, v0, 3, 3
	v_lshl_or_b32 v4, v1, 5, v2
	v_lshlrev_b32_e32 v2, 3, v0
	v_lshl_add_u32 v11, v182, 4, 0
	v_and_b32_e32 v2, 56, v2
	v_mul_u32_u24_e32 v16, 0x2020, v1
	v_mov_b32_e32 v3, 0
	v_lshl_add_u32 v27, v4, 2, 0
	v_mul_u32_u24_e32 v28, 0x404, v2
	v_lshlrev_b32_e32 v10, 6, v4
	s_add_i32 s10, 0, 0x22c38
	v_add_u32_e32 v16, v11, v16
	s_mov_b32 s3, 10
	s_mov_b32 s91, 0
	v_and_b32_e32 v13, 0xfc, v175
	v_and_b32_e32 v14, 56, v173
	v_or_b32_e32 v4, 0x200, v10
	v_mov_b32_e32 v5, v3
	v_or_b32_e32 v6, 0x400, v10
	v_mov_b32_e32 v7, v3
	v_or_b32_e32 v8, 0x600, v10
	v_mov_b32_e32 v9, v3
	v_mov_b32_e32 v15, s10
	s_movk_i32 s11, 0x17ff
	s_movk_i32 s12, 0x800
	s_mov_b32 s13, 0x1104e000
	s_movk_i32 s14, -2048
	v_add_u32_e32 v17, 0x404, v16
	v_add_u32_e32 v18, 0x40c, v16
	v_add_u32_e32 v19, 0x808, v16
	v_add_u32_e32 v20, 0xc0c, v16
	v_add_u32_e32 v21, 0xc14, v16
	v_add_u32_e32 v22, 0x1414, v16
	v_add_u32_e32 v23, 0x141c, v16
	v_add_u32_e32 v24, 0x1818, v16
	v_add_u32_e32 v25, 0x1c1c, v16
	v_add_u32_e32 v26, 0x1c24, v16
	v_lshlrev_b32_e32 v2, 1, v2
	v_add_u32_e32 v27, v27, v28
	v_lshlrev_b32_e32 v10, 1, v10
	s_branch .LBB0_1612

; #define SEAM(k) do { if (IN(k) && IN((k) + 1)) xcd_barrier(bar); \
;         if (PROBE_MASK) { const unsigned long long t_ = __builtin_amdgcn_s_memrealtime(); if ((PROBE_MASK >> (k)) & 1u) pr_acc += t_ - pr_t0; pr_t0 = t_; } } while (0)
; __device__ __forceinline__ void convert_deferred(const Ptrs& P, unsigned char* lds, int quota) {
;     const int tid = threadIdx.x, wid = tid >> 6, lane = tid & 63;
;     float* tile = (float*)lds;
;     volatile __attribute__((address_space(3))) int* slot = (volatile __attribute__((address_space(3))) int*)((__attribute__((address_space(3))) unsigned char*)lds + 131072 + 320 + 11000);
;     unsigned* q = (unsigned*)(P.ws + WS_CTL) + CW_DEFQ;
;     for (int n = 0; n < quota; ++n) {
;         __syncthreads();
;         if (tid == 0) *slot = (int)atomicAdd(q, 1u);
;         __syncthreads();
;         const int t = *slot;
;         if (t >= DEF_GU + DEF_DN) break;
;         const bool gu = t < DEF_GU;
;         const float* src = gu ? P.in[34] : P.in[36]; bf16* dst = (bf16*)(P.ws + (gu ? WS_WGU : WS_WDN));
;         const int N = gu ? 2048 : 1024, ntn = N / 256, it = gu ? 2 * NE * 16 * 8 - DEF_GU + t : 2 * NE * 16 * 4 - DEF_DN + (t - DEF_GU);
; __global__ void __launch_bounds__(NT, 2) mega(Args args) {
;     ...
;         if (IDLE_LAST(68 * 12)) convert_deferred(P, lds, 4); } SEAM(11);
.LBB0_1851:
	s_abs_i32 s0, s62
	v_cvt_f32_u32_e32 v2, s0
	s_sub_i32 s3, 0, s0
	v_readlane_b32 s56, v254, 40
	s_mov_b32 s1, 0
	v_rcp_iflag_f32_e32 v2, v2
	v_readlane_b32 s57, v254, 41
	v_mul_f32_e32 v2, 0x4f7ffffe, v2
	v_cvt_u32_f32_e32 v2, v2
	s_nop 0
	v_readfirstlane_b32 s4, v2
	s_mul_i32 s3, s3, s4
	s_mul_hi_u32 s3, s4, s3
	s_add_i32 s4, s4, s3
	s_mul_hi_u32 s3, s4, 0x330
	s_mul_i32 s3, s3, s0
	s_sub_i32 s3, 0x330, s3
	s_sub_i32 s4, s3, s0
	s_cmp_ge_u32 s3, s0
	s_cselect_b32 s3, s4, s3
	s_sub_i32 s4, s3, s0
	s_cmp_ge_u32 s3, s0
	s_cselect_b32 s0, s4, s3
	s_cmp_eq_u32 s0, 0
	s_cselect_b64 s[4:5], -1, 0
	s_cmp_lt_i32 s2, s0
	s_cselect_b64 s[6:7], -1, 0
	s_or_b64 s[4:5], s[4:5], s[6:7]
	s_and_b64 vcc, exec, s[4:5]
	s_cbranch_vccnz .LBB0_1861
	v_and_b32_e32 v2, 0x7c, v218
	v_lshlrev_b32_e32 v3, 5, v0
	s_movk_i32 s0, 0x400
	v_and_or_b32 v12, v3, s0, v2
	v_bfe_u32 v2, v0, 3, 3
	v_lshl_or_b32 v4, v1, 5, v2
	v_lshlrev_b32_e32 v2, 3, v0
	v_lshl_add_u32 v11, v182, 4, 0
	v_and_b32_e32 v2, 56, v2
	v_mul_u32_u24_e32 v16, 0x2020, v1
	v_mov_b32_e32 v3, 0
	s_waitcnt vmcnt(0)
	v_lshl_add_u32 v27, v4, 2, 0
	v_mul_u32_u24_e32 v28, 0x404, v2
	v_lshlrev_b32_e32 v10, 6, v4
	s_add_i32 s10, 0, 0x22c38
	v_add_u32_e32 v16, v11, v16
	v_and_b32_e32 v13, 0xfc, v218
	v_and_b32_e32 v14, 56, v179
	s_mov_b32 s3, 12
	s_mov_b32 s91, 0
	v_or_b32_e32 v4, 0x200, v10
	v_mov_b32_e32 v5, v3
	v_or_b32_e32 v6, 0x400, v10
	v_mov_b32_e32 v7, v3
	v_or_b32_e32 v8, 0x600, v10
	v_mov_b32_e32 v9, v3
	v_mov_b32_e32 v15, s10
	s_movk_i32 s11, 0x17ff
	s_movk_i32 s12, 0x800
	s_mov_b32 s13, 0x1104e000
	s_movk_i32 s14, -2048
	v_add_u32_e32 v17, 0x404, v16
	v_add_u32_e32 v18, 0x40c, v16
	v_add_u32_e32 v19, 0x808, v16
	v_add_u32_e32 v20, 0xc0c, v16
	v_add_u32_e32 v21, 0xc14, v16
	v_add_u32_e32 v22, 0x1414, v16
	v_add_u32_e32 v23, 0x141c, v16
	v_add_u32_e32 v24, 0x1818, v16
	v_add_u32_e32 v25, 0x1c1c, v16
	v_add_u32_e32 v26, 0x1c24, v16
	v_lshlrev_b32_e32 v2, 1, v2
	v_add_u32_e32 v27, v27, v28
	v_lshlrev_b32_e32 v10, 1, v10
	s_branch .LBB0_1854
